# c_proj_w conversion inside attention uses nt (streaming) loads and stores so it does not displace K/V lines in L2
# baseline (speedup 1.0000x reference)
.LBB3_3:
	s_cmp_gt_u32 s100, 8
	s_cbranch_scc1 .Lcw_a_done
	s_cmp_eq_u32 s100, 0
	s_cbranch_scc1 .Lcw_a_load
	v_cvt_pk_f16_f32 v252, v252, v253
	v_cvt_pk_f16_f32 v253, v254, v255
	v_lshrrev_b32_e32 v254, 1, v191
	global_store_dwordx2 v254, v[252:253], s[60:61] nt
	s_add_u32 s60, s60, 0x1000
	s_addc_u32 s61, s61, 0
	s_cmp_eq_u32 s100, 8
	s_cbranch_scc1 .Lcw_a_inc
.Lcw_a_load:
	global_load_dwordx4 v[252:255], v191, s[62:63] nt
	s_add_u32 s62, s62, 0x2000
	s_addc_u32 s63, s63, 0

.Lcw_a_done:
	s_mov_b32 s1, s97
	s_mov_b32 m0, s86
	s_add_i32 s5, s0, 0xffff2000
	ds_read_b128 v[0:3], v190 offset:32768
	ds_read_b128 v[112:115], v190 offset:40960
	buffer_load_dwordx4 v191, s[68:71], s5 offen lds
	ds_read_b128 v[4:7], v189 offset:32768
	ds_read_b128 v[116:119], v189 offset:40960
	s_add_i32 s6, s0, 0xffff4000
	s_mov_b32 m0, s85
	s_waitcnt lgkmcnt(3)
	v_mfma_f32_32x32x16_f16 v[80:95], v[0:3], v[156:159], -0.5
	s_add_i32 s7, s0, 0xffff6000
	buffer_load_dwordx4 v191, s[68:71], s6 offen lds
	s_waitcnt lgkmcnt(1)
	v_mfma_f32_32x32x16_f16 v[80:95], v[4:7], v[152:155], v[80:95]
	v_mfma_f32_32x32x16_f16 v[0:15], v[112:115], v[156:159], -0.5
	ds_read_b128 v[112:115], v188 offset:32768
	s_mov_b32 m0, s84
	s_add_i32 s9, s0, 0xffff8000
	s_add_i32 s10, s0, 0xfffea000
	v_exp_f32_e32 v182, v100
	v_exp_f32_e32 v183, v101
	s_waitcnt lgkmcnt(1)
	v_mfma_f32_32x32x16_f16 v[0:15], v[116:119], v[152:155], v[0:15]
	ds_read_b128 v[116:119], v188 offset:40960
	buffer_load_dwordx4 v191, s[68:71], s7 offen lds
	s_mov_b32 m0, s83
	v_exp_f32_e32 v192, v106
	v_exp_f32_e32 v193, v107
	v_exp_f32_e32 v194, v108
	v_exp_f32_e32 v111, v111
	s_waitcnt lgkmcnt(1)
	v_mfma_f32_32x32x16_f16 v[80:95], v[112:115], v[148:151], v[80:95]
	ds_read_b128 v[112:115], v187 offset:32768
	ds_read_b128 v[120:123], v187 offset:40960
	buffer_load_dwordx4 v191, s[68:71], s9 offen lds
	s_mov_b32 m0, s90
	ds_read_b128 v[124:127], v190 offset:32896
	ds_read_b128 v[162:165], v190 offset:41088
	buffer_load_dwordx4 v186, s[72:75], s10 offen lds
	s_add_i32 s10, s0, 0xfffec000
	s_mov_b32 m0, s89
	s_waitcnt lgkmcnt(4)
	v_mfma_f32_32x32x16_f16 v[0:15], v[116:119], v[148:151], v[0:15]
	ds_read_b128 v[116:119], v189 offset:32896
	ds_read_b128 v[166:169], v189 offset:41088
	buffer_load_dwordx4 v186, s[72:75], s10 offen lds
	s_add_i32 s10, s0, 0xfffee000
	s_mov_b32 m0, s88
	v_cvt_pk_f16_f32 v100, v218, v219
	v_cvt_pk_f16_f32 v101, v220, v221
	v_cvt_pk_f16_f32 v106, v182, v183
	s_waitcnt lgkmcnt(5)
	v_mfma_f32_32x32x16_f16 v[80:95], v[112:115], v[144:147], v[80:95]
	ds_read_b128 v[112:115], v188 offset:32896
	ds_read_b128 v[170:173], v188 offset:41088
	buffer_load_dwordx4 v186, s[72:75], s10 offen lds
	s_add_i32 s10, s0, 0xffff0000
	s_mov_b32 m0, s87
	ds_read_b128 v[174:177], v187 offset:32896
	ds_read_b128 v[178:181], v187 offset:41088
	buffer_load_dwordx4 v186, s[72:75], s10 offen lds
	s_waitcnt lgkmcnt(8)
	v_mfma_f32_32x32x16_f16 v[0:15], v[120:123], v[144:147], v[0:15]
	v_exp_f32_e32 v120, v96
	v_add_f32_e32 v96, 0, v210
	v_add_f32_e32 v96, v211, v96
	v_add_f32_e32 v96, v212, v96
	v_add_f32_e32 v96, v213, v96
	v_add_f32_e32 v96, v214, v96
	v_add_f32_e32 v96, v215, v96
	s_waitcnt lgkmcnt(7)
	v_mfma_f32_32x32x16_f16 v[80:95], v[124:127], v[140:143], v[80:95]
	v_add_f32_e32 v96, v216, v96
	v_add_f32_e32 v96, v217, v96
	v_add_f32_e32 v96, v218, v96
	v_add_f32_e32 v96, v219, v96
	v_add_f32_e32 v96, v220, v96
	v_add_f32_e32 v96, v221, v96
	v_add_f32_e32 v96, v222, v96
	v_exp_f32_e32 v121, v97
	s_waitcnt lgkmcnt(6)
	v_mfma_f32_32x32x16_f16 v[0:15], v[162:165], v[140:143], v[0:15]
	v_add_f32_e32 v96, v223, v96
	v_exp_f32_e32 v122, v98
	v_add_f32_e32 v96, v224, v96
	v_exp_f32_e32 v123, v99
	v_add_f32_e32 v96, v225, v96
	v_add_f32_e32 v96, v120, v96
	v_add_f32_e32 v96, v121, v96
	s_waitcnt lgkmcnt(5)
	v_mfma_f32_32x32x16_f16 v[80:95], v[116:119], v[136:139], v[80:95]
	v_exp_f32_e32 v124, v102
	v_add_f32_e32 v96, v122, v96
	v_exp_f32_e32 v125, v103
	v_add_f32_e32 v96, v123, v96
	v_exp_f32_e32 v126, v104
	v_add_f32_e32 v96, v182, v96
	v_exp_f32_e32 v127, v105
	s_waitcnt lgkmcnt(4)
	v_mfma_f32_32x32x16_f16 v[0:15], v[166:169], v[136:139], v[0:15]
	v_add_f32_e32 v96, v183, v96
	v_add_f32_e32 v96, v124, v96
	v_add_f32_e32 v96, v125, v96
	v_add_f32_e32 v96, v126, v96
	v_exp_f32_e32 v162, v109
	v_add_f32_e32 v96, v127, v96
	v_exp_f32_e32 v163, v110
	s_waitcnt lgkmcnt(3)
	v_mfma_f32_32x32x16_f16 v[80:95], v[112:115], v[132:135], v[80:95]
	v_add_f32_e32 v96, v192, v96
	v_add_f32_e32 v96, v193, v96
	v_add_f32_e32 v96, v194, v96
	v_add_f32_e32 v96, v162, v96
	v_add_f32_e32 v96, v163, v96
	v_add_f32_e32 v96, v111, v96
	v_mov_b32_e32 v97, v96
	s_waitcnt lgkmcnt(2)
	v_mfma_f32_32x32x16_f16 v[0:15], v[170:173], v[132:135], v[0:15]
	v_permlane32_swap_b32_e32 v96, v97
	v_add_f32_e32 v96, v96, v97
	v_add_f32_e32 v185, v185, v96
	v_cvt_pk_f16_f32 v96, v210, v211
	v_cvt_pk_f16_f32 v97, v212, v213
	v_cvt_pk_f16_f32 v98, v214, v215
	s_waitcnt lgkmcnt(1)
	v_mfma_f32_32x32x16_f16 v[80:95], v[174:177], v[128:131], v[80:95]
	v_cvt_pk_f16_f32 v99, v216, v217
	v_cvt_pk_f16_f32 v102, v222, v223
	v_cvt_pk_f16_f32 v103, v224, v225
	v_cvt_pk_f16_f32 v104, v120, v121
	v_cvt_pk_f16_f32 v105, v122, v123
	v_cvt_pk_f16_f32 v107, v124, v125
	v_cvt_pk_f16_f32 v108, v126, v127
	v_cvt_pk_f16_f32 v109, v192, v193
	v_cvt_pk_f16_f32 v110, v194, v162
	v_cvt_pk_f16_f32 v111, v163, v111
	v_permlane32_swap_b32_e32 v96, v98
	v_permlane32_swap_b32_e32 v97, v99
	v_permlane32_swap_b32_e32 v100, v102
	v_permlane32_swap_b32_e32 v101, v103
	v_permlane32_swap_b32_e32 v104, v106
	v_permlane32_swap_b32_e32 v105, v107
	v_permlane32_swap_b32_e32 v108, v110
	v_permlane32_swap_b32_e32 v109, v111
	s_waitcnt lgkmcnt(0)
	v_mfma_f32_32x32x16_f16 v[0:15], v[178:181], v[128:131], v[0:15]
	ds_read_b64_tr_b16 v[112:113], v184 offset:0
	ds_read_b64_tr_b16 v[114:115], v184 offset:0x800
	ds_read_b64_tr_b16 v[116:117], v184 offset:0x1000
	ds_read_b64_tr_b16 v[118:119], v184 offset:0x1800
	ds_read_b64_tr_b16 v[120:121], v184 offset:0x2000
	ds_read_b64_tr_b16 v[122:123], v184 offset:0x2800
	ds_read_b64_tr_b16 v[124:125], v184 offset:0x3000
	ds_read_b64_tr_b16 v[126:127], v184 offset:0x3800
	s_waitcnt lgkmcnt(0)
	s_nop 0
	v_mfma_f32_32x32x16_f16 v[64:79], v[96:99], v[112:115], v[64:79]
	v_exp_f32_e32 v208, v80
	v_exp_f32_e32 v192, v81
	ds_read_b64_tr_b16 v[80:81], v184 offset:0x200
	v_exp_f32_e32 v193, v82
	v_exp_f32_e32 v194, v83
	ds_read_b64_tr_b16 v[82:83], v184 offset:0xa00
	ds_read_b64_tr_b16 v[112:113], v184 offset:0x1200
	v_mfma_f32_32x32x16_f16 v[64:79], v[100:103], v[116:119], v[64:79]
	ds_read_b64_tr_b16 v[114:115], v184 offset:0x1a00
	ds_read_b64_tr_b16 v[116:117], v184 offset:0x2200
	ds_read_b64_tr_b16 v[118:119], v184 offset:0x2a00
	v_mfma_f32_32x32x16_f16 v[64:79], v[104:107], v[120:123], v[64:79]
	ds_read_b64_tr_b16 v[120:121], v184 offset:0x3200
	ds_read_b64_tr_b16 v[122:123], v184 offset:0x3a00
	s_waitcnt lgkmcnt(0)
	v_mfma_f32_32x32x16_f16 v[64:79], v[108:111], v[124:127], v[64:79]
	v_mfma_f32_32x32x16_f16 v[48:63], v[96:99], v[80:83], v[48:63]
	ds_read_b64_tr_b16 v[80:81], v184 offset:0x400
	ds_read_b64_tr_b16 v[82:83], v184 offset:0xc00
	v_exp_f32_e32 v195, v84
	v_exp_f32_e32 v196, v85
	ds_read_b64_tr_b16 v[84:85], v184 offset:0x1400
	v_exp_f32_e32 v197, v86
	v_exp_f32_e32 v198, v87
	v_mfma_f32_32x32x16_f16 v[48:63], v[100:103], v[112:115], v[48:63]
	ds_read_b64_tr_b16 v[86:87], v184 offset:0x1c00
	ds_read_b64_tr_b16 v[112:113], v184 offset:0x2400
	ds_read_b64_tr_b16 v[114:115], v184 offset:0x2c00
	v_mfma_f32_32x32x16_f16 v[48:63], v[104:107], v[116:119], v[48:63]
	ds_read_b64_tr_b16 v[116:117], v184 offset:0x3400
	ds_read_b64_tr_b16 v[118:119], v184 offset:0x3c00
	s_waitcnt lgkmcnt(0)
	v_mfma_f32_32x32x16_f16 v[48:63], v[108:111], v[120:123], v[48:63]
	v_mfma_f32_32x32x16_f16 v[32:47], v[96:99], v[80:83], v[32:47]
	ds_read_b64_tr_b16 v[80:81], v184 offset:0x600
	ds_read_b64_tr_b16 v[82:83], v184 offset:0xe00
	v_exp_f32_e32 v199, v88
	v_exp_f32_e32 v200, v89
	v_exp_f32_e32 v201, v90
	v_exp_f32_e32 v202, v91
	v_mfma_f32_32x32x16_f16 v[32:47], v[100:103], v[84:87], v[32:47]
	ds_read_b64_tr_b16 v[84:85], v184 offset:0x1600
	ds_read_b64_tr_b16 v[86:87], v184 offset:0x1e00
	ds_read_b64_tr_b16 v[88:89], v184 offset:0x2600
	ds_read_b64_tr_b16 v[90:91], v184 offset:0x2e00
	v_mfma_f32_32x32x16_f16 v[32:47], v[104:107], v[112:115], v[32:47]
	ds_read_b64_tr_b16 v[112:113], v184 offset:0x3600
	ds_read_b64_tr_b16 v[114:115], v184 offset:0x3e00
	s_waitcnt lgkmcnt(0)
	v_mfma_f32_32x32x16_f16 v[32:47], v[108:111], v[116:119], v[32:47]
	v_mfma_f32_32x32x16_f16 v[16:31], v[96:99], v[80:83], v[16:31]
	v_exp_f32_e32 v203, v92
	v_exp_f32_e32 v204, v93
	v_exp_f32_e32 v205, v94
	v_exp_f32_e32 v206, v95
	s_waitcnt vmcnt(0) lgkmcnt(0)
	s_barrier
	v_mfma_f32_32x32x16_f16 v[16:31], v[100:103], v[84:87], v[16:31]
	v_mfma_f32_32x32x16_f16 v[16:31], v[104:107], v[88:91], v[16:31]
	v_mfma_f32_32x32x16_f16 v[16:31], v[108:111], v[112:115], v[16:31]
	s_cmp_gt_u32 s100, 8
	s_cbranch_scc1 .Lcw_b_done
	s_cmp_eq_u32 s100, 0
	s_cbranch_scc1 .Lcw_b_load
	v_cvt_pk_f16_f32 v252, v252, v253
	v_cvt_pk_f16_f32 v253, v254, v255
	v_lshrrev_b32_e32 v254, 1, v191
	global_store_dwordx2 v254, v[252:253], s[60:61] nt
	s_add_u32 s60, s60, 0x1000
	s_addc_u32 s61, s61, 0
	s_cmp_eq_u32 s100, 8
	s_cbranch_scc1 .Lcw_b_inc
